# speedup vs baseline: 1.0632x; 1.0632x over previous
.LBB1_15:
	v_readfirstlane_b32 s86, v172
	v_readfirstlane_b32 s87, v173
	v_readfirstlane_b32 s88, v174
	v_readfirstlane_b32 s89, v175
	v_lshrrev_b32_e32 v232, 3, v198
	v_and_b32_e32 v233, 7, v198
	v_xor_b32_e32 v233, v233, v232
	s_and_b32 s84, s27, 0x7ff
	s_lshr_b32 s85, s62, 1
	s_lshl_b32 s85, s85, 7
	s_add_i32 s84, s84, s85
	s_and_b32 s85, s62, 1
	s_lshl_b32 s85, s85, 5
	s_add_i32 s84, s84, s85
	v_add_u32_e32 v232, s84, v232
	v_lshlrev_b32_e32 v232, 7, v232
	v_lshl_add_u32 v232, v233, 4, v232
	s_bfe_u32 s91, s27, 0x10006
	s_lshl_b32 s90, s91, 2
	s_add_i32 s90, s90, s62
	s_lshl_b32 s90, s90, 10
	s_add_u32 s92, s86, 0x0
	s_addc_u32 s93, s87, 0
	s_add_i32 m0, s90, 0x0
	s_nop 0
	global_load_lds_dwordx4 v232, s[92:93]
	s_add_u32 s92, s86, 0x400
	s_addc_u32 s93, s87, 0
	s_add_i32 m0, s90, 0x2000
	s_nop 0
	global_load_lds_dwordx4 v232, s[92:93]
	s_add_u32 s92, s86, 0x800
	s_addc_u32 s93, s87, 0
	s_add_i32 m0, s90, 0x4000
	s_nop 0
	global_load_lds_dwordx4 v232, s[92:93]
	s_add_u32 s92, s86, 0xc00
	s_addc_u32 s93, s87, 0
	s_add_i32 m0, s90, 0x6000
	s_nop 0
	global_load_lds_dwordx4 v232, s[92:93]
	s_add_u32 s92, s88, 0x0
	s_addc_u32 s93, s89, 0
	s_add_i32 m0, s90, 0x8000
	s_nop 0
	global_load_lds_dwordx4 v232, s[92:93]
	s_add_u32 s92, s88, 0x400
	s_addc_u32 s93, s89, 0
	s_add_i32 m0, s90, 0xa000
	s_nop 0
	global_load_lds_dwordx4 v232, s[92:93]
	s_add_u32 s92, s88, 0x800
	s_addc_u32 s93, s89, 0
	s_add_i32 m0, s90, 0xc000
	s_nop 0
	global_load_lds_dwordx4 v232, s[92:93]
	s_add_u32 s92, s88, 0xc00
	s_addc_u32 s93, s89, 0
	s_add_i32 m0, s90, 0xe000
	s_nop 0
	global_load_lds_dwordx4 v232, s[92:93]
	v_and_b32_e32 v234, 15, v198
	v_lshrrev_b32_e32 v235, 4, v198
	v_and_b32_e32 v236, 7, v234
	v_lshrrev_b32_e32 v237, 3, v234
	v_lshlrev_b32_e32 v238, 1, v235
	v_xor_b32_e32 v239, v238, v236
	v_or_b32_e32 v238, 1, v238
	v_xor_b32_e32 v238, v238, v236
	v_lshlrev_b32_e32 v237, 13, v237
	v_lshl_add_u32 v237, v236, 7, v237
	s_lshl_b32 s91, s91, 12
	v_add_u32_e32 v237, s91, v237
	v_lshl_add_u32 v244, v239, 4, v237
	v_lshl_add_u32 v245, v238, 4, v237
	s_waitcnt vmcnt(0)
	s_barrier
	s_cmp_gt_i32 s77, 7
	s_cselect_b64 s[52:53], -1, 0
	s_lshl_b32 s4, s77, 2
	s_add_i32 s78, s4, s66
	s_or_b32 s37, s4, s62
	s_lshr_b32 s4, s27, 8
	s_and_b32 s4, s4, 0x7ff8
	v_and_b32_e32 v147, 64, v198
	s_add_i32 s10, s4, s78
	s_lshr_b32 s4, s27, 6
	v_xor_b32_e32 v146, 16, v198
	v_add_u32_e32 v206, 64, v147
	s_and_b32 s4, s4, 0x7fe0
	v_cmp_lt_i32_e32 vcc, v146, v206
	s_add_i32 s54, s4, s37
	s_cmp_lt_i32 s77, 8
	v_cndmask_b32_e32 v146, v198, v146, vcc
	v_lshlrev_b32_e32 v201, 2, v146
	v_mul_f32_e32 v146, v127, v127
	v_mul_f32_e32 v147, v129, v129
	s_cselect_b64 s[6:7], -1, 0
	v_fmac_f32_e32 v146, v126, v126
	v_fmac_f32_e32 v147, v128, v128
	s_and_b64 s[4:5], s[6:7], exec
	v_add_f32_e32 v153, v146, v147
	v_pk_mul_f32 v[146:147], v[124:125], v[124:125]
	v_pk_mul_f32 v[148:149], v[122:123], v[122:123]
	s_cselect_b32 s9, s23, s25
	s_cselect_b32 s8, s22, s24
	v_and_b32_e32 v152, 0x7cf, v199
	v_mov_b32_e32 v150, v146
	v_mov_b32_e32 v151, v148
	v_mov_b32_e32 v148, v147
	global_load_dwordx4 v[138:141], v194, s[8:9] offset:16
	global_load_dwordx4 v[142:145], v194, s[8:9]
	global_load_dwordx4 v[130:133], v194, s[8:9] offset:144
	global_load_dwordx4 v[134:137], v194, s[8:9] offset:128
	v_pk_add_f32 v[146:147], v[150:151], v[148:149]
	v_lshlrev_b32_e32 v170, 7, v152
	v_add_f32_e32 v147, v153, v147
	v_add_f32_e32 v207, v146, v147
	ds_read_b128 v[146:149], v245 offset:32768
	s_nop 0
	ds_read_b128 v[150:153], v244 offset:32768
	s_nop 0
	ds_read_b128 v[154:157], v245 offset:0
	s_nop 0
	ds_read_b128 v[158:161], v244 offset:0
	v_pk_mul_f32 v[184:185], v[112:113], v[112:113]
	v_pk_mul_f32 v[202:203], v[110:111], v[110:111]
	v_mov_b32_e32 v204, v184
	v_mov_b32_e32 v205, v202
	v_mov_b32_e32 v202, v185
	v_pk_add_f32 v[184:185], v[204:205], v[202:203]
	v_pk_mul_f32 v[202:203], v[106:107], v[106:107]
	v_add_f32_e32 v170, v207, v185
	v_add_f32_e32 v170, v184, v170
	v_pk_mul_f32 v[184:185], v[108:109], v[108:109]
	v_mov_b32_e32 v205, v202
	v_mov_b32_e32 v204, v184
	v_mov_b32_e32 v202, v185
	v_pk_add_f32 v[184:185], v[204:205], v[202:203]
	v_cndmask_b32_e64 v200, 1.0, v197, s[6:7]
	v_add_f32_e32 v170, v185, v170
	v_add_f32_e32 v170, v184, v170
	v_mov_b32_e32 v184, v170
	s_nop 1
	v_permlane16_swap_b32_e32 v184, v170
	v_xor_b32_e32 v185, 32, v198
	v_cmp_lt_i32_e32 vcc, v185, v206
	s_cselect_b32 s55, s17, s19
	v_or_b32_e32 v229, 16, v199
	v_cndmask_b32_e32 v185, v198, v185, vcc
	v_lshlrev_b32_e32 v202, 2, v185
	s_waitcnt lgkmcnt(0)
	v_add_f32_e32 v170, v170, v184
	v_mov_b32_e32 v184, v170
	s_nop 1
	v_permlane32_swap_b32_e32 v184, v170
	s_waitcnt lgkmcnt(0)
	v_add_f32_e32 v170, v170, v184
	v_fmamk_f32 v170, v170, 0x3c800000, v195
	v_mul_f32_e32 v184, 0x4f800000, v170
	v_cmp_gt_f32_e32 vcc, s70, v170
	s_nop 1
	v_cndmask_b32_e32 v170, v170, v184, vcc
	v_sqrt_f32_e32 v184, v170
	s_nop 0
	v_add_u32_e32 v185, -1, v184
	v_fma_f32 v203, -v185, v184, v170
	v_cmp_ge_f32_e64 s[8:9], 0, v203
	v_add_u32_e32 v203, 1, v184
	s_nop 0
	v_cndmask_b32_e64 v185, v184, v185, s[8:9]
	v_fma_f32 v184, -v203, v184, v170
	v_cmp_lt_f32_e64 s[8:9], 0, v184
	s_nop 1
	v_cndmask_b32_e64 v184, v185, v203, s[8:9]
	v_mul_f32_e32 v185, 0x37800000, v184
	v_cndmask_b32_e32 v184, v184, v185, vcc
	v_cmp_class_f32_e32 vcc, v170, v196
	v_lshl_or_b32 v203, s10, 17, v187
	v_lshl_or_b32 v185, s54, 17, v188
	v_cndmask_b32_e32 v170, v184, v170, vcc
	v_div_scale_f32 v184, s[8:9], v170, v170, v200
	v_rcp_f32_e32 v204, v184
	s_cselect_b32 s54, s16, s18
	s_cselect_b32 s10, s72, 0x1000
	v_fma_f32 v205, -v184, v204, 1.0
	v_fmac_f32_e32 v204, v205, v204
	v_div_scale_f32 v205, vcc, v200, v170, v200
	v_mul_f32_e32 v206, v205, v204
	v_fma_f32 v207, -v184, v206, v205
	v_fmac_f32_e32 v206, v207, v204
	v_fma_f32 v184, -v184, v206, v205
	v_div_fmas_f32 v184, v184, v204, v206
	v_div_fixup_f32 v170, v184, v170, v200
	v_pk_mul_f32 v[216:217], v[106:107], v[170:171] op_sel_hi:[1,0]
	v_pk_mul_f32 v[210:211], v[122:123], v[170:171] op_sel_hi:[1,0]
	s_waitcnt vmcnt(0)
	v_pk_mul_f32 v[216:217], v[130:131], v[216:217]
	v_pk_mul_f32 v[210:211], v[138:139], v[210:211]
	v_pk_mul_f32 v[224:225], v[146:147], v[216:217]
	v_pk_mul_f32 v[212:213], v[110:111], v[170:171] op_sel_hi:[1,0]
	v_pk_fma_f32 v[224:225], v[154:155], v[210:211], v[224:225] neg_lo:[0,0,1] neg_hi:[0,0,1]
	v_pk_mul_f32 v[154:155], v[154:155], v[216:217]
	v_pk_mul_f32 v[214:215], v[112:113], v[170:171] op_sel_hi:[1,0]
	v_pk_mul_f32 v[218:219], v[108:109], v[170:171] op_sel_hi:[1,0]
	v_pk_fma_f32 v[154:155], v[146:147], v[210:211], v[154:155]
	v_lshlrev_b32_e32 v146, 6, v199
	v_pk_mul_f32 v[204:205], v[128:129], v[170:171] op_sel_hi:[1,0]
	v_pk_mul_f32 v[206:207], v[126:127], v[170:171] op_sel_hi:[1,0]
	v_pk_mul_f32 v[208:209], v[124:125], v[170:171] op_sel_hi:[1,0]
	v_pk_mul_f32 v[214:215], v[136:137], v[214:215]
	v_pk_mul_f32 v[212:213], v[134:135], v[212:213]
	v_pk_mul_f32 v[218:219], v[132:133], v[218:219]
	v_cndmask_b32_e64 v184, v203, v185, s[6:7]
	v_and_b32_e32 v228, 0x1f000, v146
	v_pk_mul_f32 v[206:207], v[142:143], v[206:207]
	v_pk_mul_f32 v[204:205], v[144:145], v[204:205]
	v_pk_mul_f32 v[208:209], v[140:141], v[208:209]
	v_pk_mul_f32 v[220:221], v[150:151], v[212:213]
	v_pk_mul_f32 v[222:223], v[152:153], v[214:215]
	v_pk_mul_f32 v[226:227], v[148:149], v[218:219]
	v_or3_b32 v146, v228, v189, v184
	v_pk_fma_f32 v[222:223], v[160:161], v[204:205], v[222:223] neg_lo:[0,0,1] neg_hi:[0,0,1]
	v_pk_fma_f32 v[220:221], v[158:159], v[206:207], v[220:221] neg_lo:[0,0,1] neg_hi:[0,0,1]
	v_pk_fma_f32 v[226:227], v[156:157], v[208:209], v[226:227] neg_lo:[0,0,1] neg_hi:[0,0,1]
	v_pk_mul_f32 v[158:159], v[158:159], v[212:213]
	v_pk_mul_f32 v[160:161], v[160:161], v[214:215]
	v_pk_mul_f32 v[156:157], v[156:157], v[218:219]
	v_ashrrev_i32_e32 v147, 31, v146
	v_pk_fma_f32 v[152:153], v[152:153], v[204:205], v[160:161]
	v_pk_fma_f32 v[150:151], v[150:151], v[206:207], v[158:159]
	v_pk_fma_f32 v[156:157], v[148:149], v[208:209], v[156:157]
	v_lshl_add_u64 v[158:159], v[146:147], 1, s[54:55]
	v_cvt_pk_f16_f32 v146, v220, v221
	v_cvt_pk_f16_f32 v147, v222, v223
	v_cvt_pk_f16_f32 v148, v224, v225
	v_cvt_pk_f16_f32 v149, v226, v227
	v_cvt_pk_f16_f32 v150, v150, v151
	v_cvt_pk_f16_f32 v151, v152, v153
	v_cvt_pk_f16_f32 v152, v154, v155
	v_cvt_pk_f16_f32 v153, v156, v157
	global_store_dwordx4 v[158:159], v[146:149], off sc1
	v_pk_mul_f32 v[204:205], v[96:97], v[96:97]
	v_pk_mul_f32 v[206:207], v[94:95], v[94:95]
	v_lshl_add_u64 v[146:147], v[158:159], 0, s[10:11]
	global_store_dwordx4 v[146:147], v[150:153], off sc1
	v_mul_f32_e32 v146, v119, v119
	v_mul_f32_e32 v147, v121, v121
	v_fmac_f32_e32 v146, v118, v118
	v_fmac_f32_e32 v147, v120, v120
	v_add_f32_e32 v153, v146, v147
	v_pk_mul_f32 v[146:147], v[116:117], v[116:117]
	v_pk_mul_f32 v[148:149], v[114:115], v[114:115]
	v_bitop3_b32 v152, v199, s73, 16 bitop3:0xc8
	v_mov_b32_e32 v150, v146
	v_mov_b32_e32 v151, v148
	v_mov_b32_e32 v148, v147
	v_pk_add_f32 v[146:147], v[150:151], v[148:149]
	v_lshlrev_b32_e32 v170, 7, v152
	v_add_f32_e32 v147, v153, v147
	v_add_f32_e32 v210, v146, v147
	ds_read_b128 v[146:149], v245 offset:49152
	s_nop 0
	ds_read_b128 v[150:153], v244 offset:49152
	s_nop 0
	ds_read_b128 v[154:157], v245 offset:16384
	s_nop 0
	ds_read_b128 v[158:161], v244 offset:16384
	v_mov_b32_e32 v208, v204
	v_mov_b32_e32 v209, v206
	v_mov_b32_e32 v206, v205
	v_pk_add_f32 v[204:205], v[208:209], v[206:207]
	v_pk_mul_f32 v[206:207], v[90:91], v[90:91]
	v_add_f32_e32 v170, v210, v205
	v_add_f32_e32 v170, v204, v170
	v_pk_mul_f32 v[204:205], v[92:93], v[92:93]
	v_mov_b32_e32 v209, v206
	v_mov_b32_e32 v208, v204
	v_mov_b32_e32 v206, v205
	v_pk_add_f32 v[204:205], v[208:209], v[206:207]
	s_nop 0
	v_add_f32_e32 v170, v205, v170
	v_add_f32_e32 v170, v204, v170
	v_mov_b32_e32 v204, v170
	s_nop 1
	v_permlane16_swap_b32_e32 v204, v170
	s_waitcnt lgkmcnt(0)
	v_add_f32_e32 v170, v170, v204
	v_mov_b32_e32 v204, v170
	s_nop 1
	v_permlane32_swap_b32_e32 v204, v170
	s_waitcnt lgkmcnt(0)
	v_add_f32_e32 v170, v170, v204
	v_fmamk_f32 v170, v170, 0x3c800000, v195
	v_mul_f32_e32 v204, 0x4f800000, v170
	v_cmp_gt_f32_e32 vcc, s70, v170
	s_nop 1
	v_cndmask_b32_e32 v170, v170, v204, vcc
	v_sqrt_f32_e32 v204, v170
	s_nop 0
	v_add_u32_e32 v205, -1, v204
	v_fma_f32 v206, -v205, v204, v170
	v_cmp_ge_f32_e64 s[8:9], 0, v206
	v_add_u32_e32 v206, 1, v204
	s_nop 0
	v_cndmask_b32_e64 v205, v204, v205, s[8:9]
	v_fma_f32 v204, -v206, v204, v170
	v_cmp_lt_f32_e64 s[8:9], 0, v204
	s_nop 1
	v_cndmask_b32_e64 v204, v205, v206, s[8:9]
	v_mul_f32_e32 v205, 0x37800000, v204
	v_cndmask_b32_e32 v204, v204, v205, vcc
	v_cmp_class_f32_e32 vcc, v170, v196
	s_nop 1
	v_cndmask_b32_e32 v170, v204, v170, vcc
	v_div_scale_f32 v204, s[8:9], v170, v170, v200
	v_rcp_f32_e32 v205, v204
	s_mov_b64 s[8:9], -1
	v_fma_f32 v206, -v204, v205, 1.0
	v_fmac_f32_e32 v205, v206, v205
	v_div_scale_f32 v206, vcc, v200, v170, v200
	v_mul_f32_e32 v207, v206, v205
	v_fma_f32 v208, -v204, v207, v206
	v_fmac_f32_e32 v207, v208, v205
	v_fma_f32 v204, -v204, v207, v206
	v_div_fmas_f32 v204, v204, v205, v207
	v_div_fixup_f32 v170, v204, v170, v200
	v_pk_mul_f32 v[216:217], v[90:91], v[170:171] op_sel_hi:[1,0]
	v_pk_mul_f32 v[210:211], v[114:115], v[170:171] op_sel_hi:[1,0]
	v_pk_mul_f32 v[216:217], v[130:131], v[216:217]
	v_pk_mul_f32 v[210:211], v[138:139], v[210:211]
	v_pk_mul_f32 v[212:213], v[94:95], v[170:171] op_sel_hi:[1,0]
	v_pk_mul_f32 v[214:215], v[96:97], v[170:171] op_sel_hi:[1,0]
	s_waitcnt lgkmcnt(0)
	v_pk_mul_f32 v[224:225], v[146:147], v[216:217]
	v_pk_mul_f32 v[218:219], v[92:93], v[170:171] op_sel_hi:[1,0]
	s_waitcnt lgkmcnt(0)
	v_pk_fma_f32 v[224:225], v[154:155], v[210:211], v[224:225] neg_lo:[0,0,1] neg_hi:[0,0,1]
	v_pk_mul_f32 v[154:155], v[154:155], v[216:217]
	v_pk_mul_f32 v[204:205], v[120:121], v[170:171] op_sel_hi:[1,0]
	v_pk_fma_f32 v[154:155], v[146:147], v[210:211], v[154:155]
	v_lshlrev_b32_e32 v146, 3, v229
	v_pk_mul_f32 v[206:207], v[118:119], v[170:171] op_sel_hi:[1,0]
	v_pk_mul_f32 v[208:209], v[116:117], v[170:171] op_sel_hi:[1,0]
	v_pk_mul_f32 v[214:215], v[136:137], v[214:215]
	v_pk_mul_f32 v[212:213], v[134:135], v[212:213]
	v_pk_mul_f32 v[218:219], v[132:133], v[218:219]
	v_and_b32_e32 v146, 0xf8, v146
	v_pk_mul_f32 v[206:207], v[142:143], v[206:207]
	v_pk_mul_f32 v[204:205], v[144:145], v[204:205]
	v_pk_mul_f32 v[208:209], v[140:141], v[208:209]
	v_pk_mul_f32 v[220:221], v[150:151], v[212:213]
	v_pk_mul_f32 v[222:223], v[152:153], v[214:215]
	v_pk_mul_f32 v[226:227], v[148:149], v[218:219]
	v_or3_b32 v146, v228, v146, v184
	s_waitcnt lgkmcnt(0)
	v_pk_fma_f32 v[222:223], v[160:161], v[204:205], v[222:223] neg_lo:[0,0,1] neg_hi:[0,0,1]
	v_pk_fma_f32 v[220:221], v[158:159], v[206:207], v[220:221] neg_lo:[0,0,1] neg_hi:[0,0,1]
	v_pk_fma_f32 v[226:227], v[156:157], v[208:209], v[226:227] neg_lo:[0,0,1] neg_hi:[0,0,1]
	v_pk_mul_f32 v[158:159], v[158:159], v[212:213]
	v_pk_mul_f32 v[160:161], v[160:161], v[214:215]
	v_pk_mul_f32 v[156:157], v[156:157], v[218:219]
	v_ashrrev_i32_e32 v147, 31, v146
	v_pk_fma_f32 v[152:153], v[152:153], v[204:205], v[160:161]
	v_pk_fma_f32 v[150:151], v[150:151], v[206:207], v[158:159]
	v_pk_fma_f32 v[156:157], v[148:149], v[208:209], v[156:157]
	v_lshl_add_u64 v[158:159], v[146:147], 1, s[54:55]
	v_cvt_pk_f16_f32 v146, v220, v221
	v_cvt_pk_f16_f32 v147, v222, v223
	v_cvt_pk_f16_f32 v148, v224, v225
	v_cvt_pk_f16_f32 v149, v226, v227
	v_bitop3_b32 v184, v199, s74, 32 bitop3:0xc8
	v_cvt_pk_f16_f32 v150, v150, v151
	v_cvt_pk_f16_f32 v151, v152, v153
	v_cvt_pk_f16_f32 v152, v154, v155
	v_cvt_pk_f16_f32 v153, v156, v157
	global_store_dwordx4 v[158:159], v[146:149], off sc1
	v_lshlrev_b32_e32 v170, 7, v184
	v_mul_f32_e32 v204, v105, v105
	v_lshl_add_u64 v[146:147], v[158:159], 0, s[10:11]
	global_store_dwordx4 v[146:147], v[150:153], off sc1
	v_fmac_f32_e32 v204, v104, v104
	ds_read_b128 v[146:149], v245 offset:1024
	ds_read_b128 v[154:157], v244 offset:1024
	s_nop 0
	ds_read_b128 v[150:153], v245 offset:33792
	s_nop 0
	ds_read_b128 v[158:161], v244 offset:33792
	v_mul_f32_e32 v170, v103, v103
	v_fmac_f32_e32 v170, v102, v102
	v_add_f32_e32 v170, v170, v204
	v_pk_mul_f32 v[204:205], v[100:101], v[100:101]
	v_pk_mul_f32 v[206:207], v[98:99], v[98:99]
	v_mov_b32_e32 v208, v204
	v_mov_b32_e32 v209, v206
	v_mov_b32_e32 v206, v205
	v_pk_add_f32 v[204:205], v[208:209], v[206:207]
	v_pk_mul_f32 v[206:207], v[78:79], v[78:79]
	v_add_f32_e32 v170, v170, v205
	v_add_f32_e32 v170, v204, v170
	v_pk_mul_f32 v[204:205], v[80:81], v[80:81]
	v_mov_b32_e32 v209, v206
	v_mov_b32_e32 v208, v204
	v_mov_b32_e32 v206, v205
	v_pk_add_f32 v[204:205], v[208:209], v[206:207]
	v_pk_mul_f32 v[206:207], v[74:75], v[74:75]
	v_add_f32_e32 v170, v170, v205
	v_add_f32_e32 v170, v204, v170
	v_pk_mul_f32 v[204:205], v[76:77], v[76:77]
	v_mov_b32_e32 v209, v206
	v_mov_b32_e32 v208, v204
	v_mov_b32_e32 v206, v205
	v_pk_add_f32 v[204:205], v[208:209], v[206:207]
	s_mov_b64 vcc, s[4:5]
	v_add_f32_e32 v170, v205, v170
	v_add_f32_e32 v170, v204, v170
	v_mov_b32_e32 v204, v170
	s_nop 1
	v_permlane16_swap_b32_e32 v204, v170
	v_lshlrev_b32_e32 v205, 6, v184
	s_waitcnt lgkmcnt(0)
	v_add_f32_e32 v170, v170, v204
	v_mov_b32_e32 v204, v170
	s_nop 1
	v_permlane32_swap_b32_e32 v204, v170
	s_cbranch_vccnz .LBB1_17
	v_or_b32_e32 v184, 32, v199
	v_lshlrev_b32_e32 v184, 3, v184
	v_and_b32_e32 v206, 0x1f000, v205
	v_and_b32_e32 v184, 0x178, v184
	v_or3_b32 v184, v206, v184, v203
	s_mov_b64 s[8:9], 0

.LBB1_20:
	s_waitcnt lgkmcnt(0)
	v_add_f32_e32 v170, v170, v204
	v_fmamk_f32 v170, v170, 0x3c800000, v195
	v_mul_f32_e32 v185, 0x4f800000, v170
	v_cmp_gt_f32_e32 vcc, s70, v170
	s_lshl_b32 s10, s56, 1
	v_add_u32_e32 v228, 0x80, v199
	v_cndmask_b32_e32 v170, v170, v185, vcc
	v_sqrt_f32_e32 v185, v170
	s_nop 0
	v_add_u32_e32 v204, -1, v185
	v_fma_f32 v206, -v204, v185, v170
	v_add_u32_e32 v205, 1, v185
	v_cmp_ge_f32_e64 s[4:5], 0, v206
	s_nop 1
	v_cndmask_b32_e64 v204, v185, v204, s[4:5]
	v_fma_f32 v185, -v205, v185, v170
	v_cmp_lt_f32_e64 s[4:5], 0, v185
	s_nop 1
	v_cndmask_b32_e64 v185, v204, v205, s[4:5]
	v_mul_f32_e32 v204, 0x37800000, v185
	v_cndmask_b32_e32 v185, v185, v204, vcc
	v_cmp_class_f32_e32 vcc, v170, v196
	s_nop 1
	v_cndmask_b32_e32 v170, v185, v170, vcc
	v_div_scale_f32 v185, s[4:5], v170, v170, v200
	v_rcp_f32_e32 v204, v185
	s_nop 0
	v_fma_f32 v205, -v185, v204, 1.0
	v_fmac_f32_e32 v204, v205, v204
	v_div_scale_f32 v205, vcc, v200, v170, v200
	v_mul_f32_e32 v206, v205, v204
	v_fma_f32 v207, -v185, v206, v205
	v_fmac_f32_e32 v206, v207, v204
	v_fma_f32 v185, -v185, v206, v205
	v_div_fmas_f32 v185, v185, v204, v206
	v_div_fixup_f32 v170, v185, v170, v200
	v_pk_mul_f32 v[212:213], v[78:79], v[170:171] op_sel_hi:[1,0]
	v_pk_mul_f32 v[214:215], v[80:81], v[170:171] op_sel_hi:[1,0]
	v_pk_mul_f32 v[216:217], v[74:75], v[170:171] op_sel_hi:[1,0]
	v_pk_mul_f32 v[218:219], v[76:77], v[170:171] op_sel_hi:[1,0]
	v_pk_mul_f32 v[204:205], v[104:105], v[170:171] op_sel_hi:[1,0]
	v_pk_mul_f32 v[206:207], v[102:103], v[170:171] op_sel_hi:[1,0]
	v_pk_mul_f32 v[208:209], v[100:101], v[170:171] op_sel_hi:[1,0]
	v_pk_mul_f32 v[210:211], v[98:99], v[170:171] op_sel_hi:[1,0]
	v_pk_mul_f32 v[214:215], v[136:137], v[214:215]
	v_pk_mul_f32 v[212:213], v[134:135], v[212:213]
	v_pk_mul_f32 v[218:219], v[132:133], v[218:219]
	v_pk_mul_f32 v[216:217], v[130:131], v[216:217]
	v_pk_mul_f32 v[206:207], v[142:143], v[206:207]
	v_pk_mul_f32 v[204:205], v[144:145], v[204:205]
	v_pk_mul_f32 v[210:211], v[138:139], v[210:211]
	v_pk_mul_f32 v[208:209], v[140:141], v[208:209]
	s_waitcnt lgkmcnt(0)
	v_pk_mul_f32 v[220:221], v[158:159], v[212:213]
	v_pk_mul_f32 v[222:223], v[160:161], v[214:215]
	v_pk_mul_f32 v[224:225], v[150:151], v[216:217]
	v_pk_mul_f32 v[226:227], v[152:153], v[218:219]
	v_pk_fma_f32 v[222:223], v[156:157], v[204:205], v[222:223] neg_lo:[0,0,1] neg_hi:[0,0,1]
	v_pk_fma_f32 v[220:221], v[154:155], v[206:207], v[220:221] neg_lo:[0,0,1] neg_hi:[0,0,1]
	v_pk_fma_f32 v[226:227], v[148:149], v[208:209], v[226:227] neg_lo:[0,0,1] neg_hi:[0,0,1]
	v_pk_fma_f32 v[224:225], v[146:147], v[210:211], v[224:225] neg_lo:[0,0,1] neg_hi:[0,0,1]
	v_pk_mul_f32 v[154:155], v[154:155], v[212:213]
	v_pk_mul_f32 v[156:157], v[156:157], v[214:215]
	v_pk_mul_f32 v[146:147], v[146:147], v[216:217]
	v_pk_mul_f32 v[148:149], v[148:149], v[218:219]
	v_ashrrev_i32_e32 v185, 31, v184
	v_pk_fma_f32 v[156:157], v[160:161], v[204:205], v[156:157]
	v_pk_fma_f32 v[154:155], v[158:159], v[206:207], v[154:155]
	v_pk_fma_f32 v[158:159], v[152:153], v[208:209], v[148:149]
	v_pk_fma_f32 v[152:153], v[150:151], v[210:211], v[146:147]
	v_lshl_add_u64 v[160:161], v[184:185], 1, s[8:9]
	v_cvt_pk_f16_f32 v146, v220, v221
	v_cvt_pk_f16_f32 v147, v222, v223
	v_cvt_pk_f16_f32 v148, v224, v225
	v_cvt_pk_f16_f32 v149, v226, v227
	v_cvt_pk_f16_f32 v150, v154, v155
	v_cvt_pk_f16_f32 v151, v156, v157
	v_cvt_pk_f16_f32 v152, v152, v153
	v_cvt_pk_f16_f32 v153, v158, v159
	global_store_dwordx4 v[160:161], v[146:149], off sc1
	v_bitop3_b32 v226, v199, s75, 48 bitop3:0xc8
	v_lshlrev_b32_e32 v170, 7, v226
	v_lshl_add_u64 v[146:147], v[160:161], 0, s[10:11]
	global_store_dwordx4 v[146:147], v[150:153], off sc1
	v_mul_f32_e32 v146, v87, v87
	v_mul_f32_e32 v147, v89, v89
	v_fmac_f32_e32 v146, v86, v86
	v_fmac_f32_e32 v147, v88, v88
	v_add_f32_e32 v152, v146, v147
	v_pk_mul_f32 v[146:147], v[84:85], v[84:85]
	v_pk_mul_f32 v[148:149], v[82:83], v[82:83]
	v_mov_b32_e32 v150, v146
	v_mov_b32_e32 v151, v148
	v_mov_b32_e32 v148, v147
	v_pk_add_f32 v[146:147], v[150:151], v[148:149]
	v_add_f32_e32 v147, v152, v147
	v_add_f32_e32 v208, v146, v147
	ds_read_b128 v[146:149], v245 offset:50176
	s_nop 0
	ds_read_b128 v[150:153], v244 offset:50176
	s_nop 0
	ds_read_b128 v[154:157], v245 offset:17408
	s_nop 0
	ds_read_b128 v[158:161], v244 offset:17408
	v_pk_mul_f32 v[184:185], v[72:73], v[72:73]
	v_pk_mul_f32 v[204:205], v[70:71], v[70:71]
	v_mov_b32_e32 v206, v184
	v_mov_b32_e32 v207, v204
	v_mov_b32_e32 v204, v185
	v_pk_add_f32 v[184:185], v[206:207], v[204:205]
	v_pk_mul_f32 v[204:205], v[66:67], v[66:67]
	v_add_f32_e32 v170, v208, v185
	v_add_f32_e32 v170, v184, v170
	v_pk_mul_f32 v[184:185], v[68:69], v[68:69]
	v_mov_b32_e32 v207, v204
	v_mov_b32_e32 v206, v184
	v_mov_b32_e32 v204, v185
	v_pk_add_f32 v[184:185], v[206:207], v[204:205]
	v_or_b32_e32 v227, 48, v199
	v_add_f32_e32 v170, v185, v170
	v_add_f32_e32 v170, v184, v170
	v_mov_b32_e32 v184, v170
	s_nop 1
	v_permlane16_swap_b32_e32 v184, v170
	s_waitcnt lgkmcnt(0)
	v_add_f32_e32 v170, v170, v184
	v_mov_b32_e32 v184, v170
	s_nop 1
	v_permlane32_swap_b32_e32 v184, v170
	s_waitcnt lgkmcnt(0)
	v_add_f32_e32 v170, v170, v184
	v_fmamk_f32 v170, v170, 0x3c800000, v195
	v_mul_f32_e32 v184, 0x4f800000, v170
	v_cmp_gt_f32_e32 vcc, s70, v170
	s_nop 1
	v_cndmask_b32_e32 v170, v170, v184, vcc
	v_sqrt_f32_e32 v184, v170
	s_nop 0
	v_add_u32_e32 v185, -1, v184
	v_fma_f32 v204, -v185, v184, v170
	v_cmp_ge_f32_e64 s[4:5], 0, v204
	v_add_u32_e32 v204, 1, v184
	s_nop 0
	v_cndmask_b32_e64 v185, v184, v185, s[4:5]
	v_fma_f32 v184, -v204, v184, v170
	v_cmp_lt_f32_e64 s[4:5], 0, v184
	s_nop 1
	v_cndmask_b32_e64 v184, v185, v204, s[4:5]
	v_mul_f32_e32 v185, 0x37800000, v184
	v_cndmask_b32_e32 v184, v184, v185, vcc
	v_cmp_class_f32_e32 vcc, v170, v196
	s_nop 1
	v_cndmask_b32_e32 v170, v184, v170, vcc
	v_div_scale_f32 v184, s[4:5], v170, v170, v200
	v_rcp_f32_e32 v185, v184
	s_nop 0
	v_fma_f32 v204, -v184, v185, 1.0
	v_fmac_f32_e32 v185, v204, v185
	v_div_scale_f32 v204, vcc, v200, v170, v200
	v_mul_f32_e32 v205, v204, v185
	v_fma_f32 v206, -v184, v205, v204
	v_fmac_f32_e32 v205, v206, v185
	v_fma_f32 v184, -v184, v205, v204
	v_div_fmas_f32 v184, v184, v185, v205
	v_div_fixup_f32 v170, v184, v170, v200
	v_pk_mul_f32 v[214:215], v[66:67], v[170:171] op_sel_hi:[1,0]
	v_pk_mul_f32 v[208:209], v[82:83], v[170:171] op_sel_hi:[1,0]
	v_pk_mul_f32 v[214:215], v[130:131], v[214:215]
	v_pk_mul_f32 v[208:209], v[138:139], v[208:209]
	s_waitcnt lgkmcnt(0)
	v_pk_mul_f32 v[222:223], v[146:147], v[214:215]
	v_pk_mul_f32 v[210:211], v[70:71], v[170:171] op_sel_hi:[1,0]
	s_waitcnt lgkmcnt(0)
	v_pk_fma_f32 v[222:223], v[154:155], v[208:209], v[222:223] neg_lo:[0,0,1] neg_hi:[0,0,1]
	v_pk_mul_f32 v[154:155], v[154:155], v[214:215]
	v_pk_mul_f32 v[212:213], v[72:73], v[170:171] op_sel_hi:[1,0]
	v_pk_mul_f32 v[216:217], v[68:69], v[170:171] op_sel_hi:[1,0]
	v_pk_fma_f32 v[154:155], v[146:147], v[208:209], v[154:155]
	v_lshlrev_b32_e32 v146, 6, v226
	v_lshlrev_b32_e32 v147, 3, v227
	v_pk_mul_f32 v[184:185], v[88:89], v[170:171] op_sel_hi:[1,0]
	v_pk_mul_f32 v[204:205], v[86:87], v[170:171] op_sel_hi:[1,0]
	v_pk_mul_f32 v[206:207], v[84:85], v[170:171] op_sel_hi:[1,0]
	v_pk_mul_f32 v[212:213], v[136:137], v[212:213]
	v_pk_mul_f32 v[210:211], v[134:135], v[210:211]
	v_pk_mul_f32 v[216:217], v[132:133], v[216:217]
	v_and_b32_e32 v146, s79, v146
	v_and_b32_e32 v147, s57, v147
	v_pk_mul_f32 v[204:205], v[142:143], v[204:205]
	v_pk_mul_f32 v[184:185], v[144:145], v[184:185]
	v_pk_mul_f32 v[206:207], v[140:141], v[206:207]
	v_pk_mul_f32 v[218:219], v[150:151], v[210:211]
	v_pk_mul_f32 v[220:221], v[152:153], v[212:213]
	v_pk_mul_f32 v[224:225], v[148:149], v[216:217]
	v_or3_b32 v146, v147, v203, v146
	s_waitcnt lgkmcnt(0)
	v_pk_fma_f32 v[220:221], v[160:161], v[184:185], v[220:221] neg_lo:[0,0,1] neg_hi:[0,0,1]
	v_pk_fma_f32 v[218:219], v[158:159], v[204:205], v[218:219] neg_lo:[0,0,1] neg_hi:[0,0,1]
	v_pk_fma_f32 v[224:225], v[156:157], v[206:207], v[224:225] neg_lo:[0,0,1] neg_hi:[0,0,1]
	v_pk_mul_f32 v[158:159], v[158:159], v[210:211]
	v_pk_mul_f32 v[160:161], v[160:161], v[212:213]
	v_pk_mul_f32 v[156:157], v[156:157], v[216:217]
	v_ashrrev_i32_e32 v147, 31, v146
	v_pk_fma_f32 v[152:153], v[152:153], v[184:185], v[160:161]
	v_pk_fma_f32 v[150:151], v[150:151], v[204:205], v[158:159]
	v_pk_fma_f32 v[156:157], v[148:149], v[206:207], v[156:157]
	v_lshl_add_u64 v[158:159], v[146:147], 1, s[8:9]
	v_cvt_pk_f16_f32 v146, v218, v219
	v_cvt_pk_f16_f32 v147, v220, v221
	v_cvt_pk_f16_f32 v148, v222, v223
	v_cvt_pk_f16_f32 v149, v224, v225
	v_cvt_pk_f16_f32 v150, v150, v151
	v_cvt_pk_f16_f32 v151, v152, v153
	v_cvt_pk_f16_f32 v152, v154, v155
	v_cvt_pk_f16_f32 v153, v156, v157
	global_store_dwordx4 v[158:159], v[146:149], off sc1
	v_pk_mul_f32 v[184:185], v[48:49], v[48:49]
	v_pk_mul_f32 v[204:205], v[46:47], v[46:47]
	v_lshl_add_u64 v[146:147], v[158:159], 0, s[10:11]
	global_store_dwordx4 v[146:147], v[150:153], off sc1
	v_mul_f32_e32 v146, v63, v63
	v_mul_f32_e32 v147, v65, v65
	v_fmac_f32_e32 v146, v62, v62
	v_fmac_f32_e32 v147, v64, v64
	v_add_f32_e32 v153, v146, v147
	v_pk_mul_f32 v[146:147], v[60:61], v[60:61]
	v_pk_mul_f32 v[148:149], v[58:59], v[58:59]
	v_and_b32_e32 v152, 0x7cf, v228
	v_mov_b32_e32 v150, v146
	v_mov_b32_e32 v151, v148
	v_mov_b32_e32 v148, v147
	v_pk_add_f32 v[146:147], v[150:151], v[148:149]
	v_lshlrev_b32_e32 v170, 7, v152
	v_add_f32_e32 v147, v153, v147
	v_add_f32_e32 v203, v146, v147
	ds_read_b128 v[146:149], v245 offset:34816
	s_nop 0
	ds_read_b128 v[150:153], v244 offset:34816
	s_nop 0
	ds_read_b128 v[154:157], v245 offset:2048
	s_nop 0
	ds_read_b128 v[158:161], v244 offset:2048
	v_mov_b32_e32 v206, v184
	v_mov_b32_e32 v207, v204
	v_mov_b32_e32 v204, v185
	v_pk_add_f32 v[184:185], v[206:207], v[204:205]
	v_pk_mul_f32 v[204:205], v[42:43], v[42:43]
	v_add_f32_e32 v170, v203, v185
	v_add_f32_e32 v170, v184, v170
	v_pk_mul_f32 v[184:185], v[44:45], v[44:45]
	v_mov_b32_e32 v207, v204
	v_mov_b32_e32 v206, v184
	v_mov_b32_e32 v204, v185
	v_pk_add_f32 v[184:185], v[206:207], v[204:205]
	s_nop 0
	v_add_f32_e32 v170, v185, v170
	v_add_f32_e32 v170, v184, v170
	v_mov_b32_e32 v184, v170
	s_nop 1
	v_permlane16_swap_b32_e32 v184, v170
	v_lshrrev_b32_e32 v185, 8, v228
	v_and_b32_e32 v185, 0x7ff8, v185
	v_add_u32_e32 v185, s78, v185
	v_lshl_or_b32 v203, v185, 17, v187
	s_waitcnt lgkmcnt(0)
	v_add_f32_e32 v170, v170, v184
	v_mov_b32_e32 v184, v170
	s_nop 1
	v_permlane32_swap_b32_e32 v184, v170
	v_lshrrev_b32_e32 v185, 6, v228
	v_and_b32_e32 v185, 0x7fe0, v185
	v_add_u32_e32 v185, s37, v185
	v_lshl_or_b32 v185, v185, 17, v188
	s_waitcnt lgkmcnt(0)
	v_add_f32_e32 v170, v170, v184
	v_fmamk_f32 v170, v170, 0x3c800000, v195
	v_mul_f32_e32 v184, 0x4f800000, v170
	v_cmp_gt_f32_e32 vcc, s70, v170
	s_nop 1
	v_cndmask_b32_e32 v170, v170, v184, vcc
	v_sqrt_f32_e32 v184, v170
	s_nop 0
	v_add_u32_e32 v204, -1, v184
	v_fma_f32 v205, -v204, v184, v170
	v_cmp_ge_f32_e64 s[4:5], 0, v205
	v_add_u32_e32 v205, 1, v184
	s_nop 0
	v_cndmask_b32_e64 v204, v184, v204, s[4:5]
	v_fma_f32 v184, -v205, v184, v170
	v_cmp_lt_f32_e64 s[4:5], 0, v184
	s_nop 1
	v_cndmask_b32_e64 v184, v204, v205, s[4:5]
	v_mul_f32_e32 v204, 0x37800000, v184
	v_cndmask_b32_e32 v184, v184, v204, vcc
	v_cmp_class_f32_e32 vcc, v170, v196
	s_nop 1
	v_cndmask_b32_e32 v170, v184, v170, vcc
	v_div_scale_f32 v184, s[4:5], v170, v170, v200
	v_rcp_f32_e32 v204, v184
	s_nop 0
	v_fma_f32 v205, -v184, v204, 1.0
	v_fmac_f32_e32 v204, v205, v204
	v_div_scale_f32 v205, vcc, v200, v170, v200
	v_mul_f32_e32 v206, v205, v204
	v_fma_f32 v207, -v184, v206, v205
	v_fmac_f32_e32 v206, v207, v204
	v_fma_f32 v184, -v184, v206, v205
	v_div_fmas_f32 v184, v184, v204, v206
	v_div_fixup_f32 v170, v184, v170, v200
	v_pk_mul_f32 v[216:217], v[42:43], v[170:171] op_sel_hi:[1,0]
	v_pk_mul_f32 v[210:211], v[58:59], v[170:171] op_sel_hi:[1,0]
	v_pk_mul_f32 v[216:217], v[130:131], v[216:217]
	v_pk_mul_f32 v[210:211], v[138:139], v[210:211]
	v_pk_mul_f32 v[212:213], v[46:47], v[170:171] op_sel_hi:[1,0]
	v_pk_mul_f32 v[214:215], v[48:49], v[170:171] op_sel_hi:[1,0]
	s_waitcnt lgkmcnt(0)
	v_pk_mul_f32 v[224:225], v[146:147], v[216:217]
	v_pk_mul_f32 v[218:219], v[44:45], v[170:171] op_sel_hi:[1,0]
	s_waitcnt lgkmcnt(0)
	v_pk_fma_f32 v[224:225], v[154:155], v[210:211], v[224:225] neg_lo:[0,0,1] neg_hi:[0,0,1]
	v_pk_mul_f32 v[154:155], v[154:155], v[216:217]
	v_pk_mul_f32 v[204:205], v[64:65], v[170:171] op_sel_hi:[1,0]
	v_pk_fma_f32 v[154:155], v[146:147], v[210:211], v[154:155]
	v_lshlrev_b32_e32 v146, 6, v228
	v_pk_mul_f32 v[206:207], v[62:63], v[170:171] op_sel_hi:[1,0]
	v_pk_mul_f32 v[208:209], v[60:61], v[170:171] op_sel_hi:[1,0]
	v_pk_mul_f32 v[214:215], v[136:137], v[214:215]
	v_pk_mul_f32 v[212:213], v[134:135], v[212:213]
	v_pk_mul_f32 v[218:219], v[132:133], v[218:219]
	v_cndmask_b32_e64 v184, v203, v185, s[6:7]
	v_and_b32_e32 v146, 0x1f000, v146
	v_pk_mul_f32 v[206:207], v[142:143], v[206:207]
	v_pk_mul_f32 v[204:205], v[144:145], v[204:205]
	v_pk_mul_f32 v[208:209], v[140:141], v[208:209]
	v_pk_mul_f32 v[220:221], v[150:151], v[212:213]
	v_pk_mul_f32 v[222:223], v[152:153], v[214:215]
	v_pk_mul_f32 v[226:227], v[148:149], v[218:219]
	v_or3_b32 v146, v146, v189, v184
	s_waitcnt lgkmcnt(0)
	v_pk_fma_f32 v[222:223], v[160:161], v[204:205], v[222:223] neg_lo:[0,0,1] neg_hi:[0,0,1]
	v_pk_fma_f32 v[220:221], v[158:159], v[206:207], v[220:221] neg_lo:[0,0,1] neg_hi:[0,0,1]
	v_pk_fma_f32 v[226:227], v[156:157], v[208:209], v[226:227] neg_lo:[0,0,1] neg_hi:[0,0,1]
	v_pk_mul_f32 v[158:159], v[158:159], v[212:213]
	v_pk_mul_f32 v[160:161], v[160:161], v[214:215]
	v_pk_mul_f32 v[156:157], v[156:157], v[218:219]
	v_ashrrev_i32_e32 v147, 31, v146
	v_pk_fma_f32 v[152:153], v[152:153], v[204:205], v[160:161]
	v_pk_fma_f32 v[150:151], v[150:151], v[206:207], v[158:159]
	v_pk_fma_f32 v[156:157], v[148:149], v[208:209], v[156:157]
	v_lshl_add_u64 v[158:159], v[146:147], 1, s[54:55]
	v_cvt_pk_f16_f32 v146, v220, v221
	v_cvt_pk_f16_f32 v147, v222, v223
	v_cvt_pk_f16_f32 v148, v224, v225
	v_cvt_pk_f16_f32 v149, v226, v227
	v_cvt_pk_f16_f32 v150, v150, v151
	v_cvt_pk_f16_f32 v151, v152, v153
	v_cvt_pk_f16_f32 v152, v154, v155
	v_cvt_pk_f16_f32 v153, v156, v157
	global_store_dwordx4 v[158:159], v[146:149], off sc1
	v_add_u32_e32 v228, 0x90, v199
	v_pk_mul_f32 v[204:205], v[32:33], v[32:33]
	v_lshl_add_u64 v[146:147], v[158:159], 0, s[10:11]
	global_store_dwordx4 v[146:147], v[150:153], off sc1
	v_mul_f32_e32 v146, v55, v55
	v_mul_f32_e32 v147, v57, v57
	v_fmac_f32_e32 v146, v54, v54
	v_fmac_f32_e32 v147, v56, v56
	v_add_f32_e32 v153, v146, v147
	v_pk_mul_f32 v[146:147], v[52:53], v[52:53]
	v_pk_mul_f32 v[148:149], v[50:51], v[50:51]
	v_and_b32_e32 v152, 0x7df, v228
	v_mov_b32_e32 v150, v146
	v_mov_b32_e32 v151, v148
	v_mov_b32_e32 v148, v147
	v_pk_add_f32 v[146:147], v[150:151], v[148:149]
	v_lshlrev_b32_e32 v170, 7, v152
	v_add_f32_e32 v147, v153, v147
	v_add_f32_e32 v210, v146, v147
	ds_read_b128 v[146:149], v245 offset:51200
	s_nop 0
	ds_read_b128 v[150:153], v244 offset:51200
	s_nop 0
	ds_read_b128 v[154:157], v245 offset:18432
	s_nop 0
	ds_read_b128 v[158:161], v244 offset:18432
	v_pk_mul_f32 v[206:207], v[30:31], v[30:31]
	v_mov_b32_e32 v208, v204
	v_mov_b32_e32 v209, v206
	v_mov_b32_e32 v206, v205
	v_pk_add_f32 v[204:205], v[208:209], v[206:207]
	v_pk_mul_f32 v[206:207], v[26:27], v[26:27]
	v_add_f32_e32 v170, v210, v205
	v_add_f32_e32 v170, v204, v170
	v_pk_mul_f32 v[204:205], v[28:29], v[28:29]
	v_mov_b32_e32 v209, v206
	v_mov_b32_e32 v208, v204
	v_mov_b32_e32 v206, v205
	v_pk_add_f32 v[204:205], v[208:209], v[206:207]
	s_nop 0
	v_add_f32_e32 v170, v205, v170
	v_add_f32_e32 v170, v204, v170
	v_mov_b32_e32 v204, v170
	s_nop 1
	v_permlane16_swap_b32_e32 v204, v170
	s_waitcnt lgkmcnt(0)
	v_add_f32_e32 v170, v170, v204
	v_mov_b32_e32 v204, v170
	s_nop 1
	v_permlane32_swap_b32_e32 v204, v170
	s_waitcnt lgkmcnt(0)
	v_add_f32_e32 v170, v170, v204
	v_fmamk_f32 v170, v170, 0x3c800000, v195
	v_mul_f32_e32 v204, 0x4f800000, v170
	v_cmp_gt_f32_e32 vcc, s70, v170
	s_nop 1
	v_cndmask_b32_e32 v170, v170, v204, vcc
	v_sqrt_f32_e32 v204, v170
	s_nop 0
	v_add_u32_e32 v205, -1, v204
	v_fma_f32 v206, -v205, v204, v170
	v_cmp_ge_f32_e64 s[4:5], 0, v206
	v_add_u32_e32 v206, 1, v204
	s_nop 0
	v_cndmask_b32_e64 v205, v204, v205, s[4:5]
	v_fma_f32 v204, -v206, v204, v170
	v_cmp_lt_f32_e64 s[4:5], 0, v204
	s_nop 1
	v_cndmask_b32_e64 v204, v205, v206, s[4:5]
	v_mul_f32_e32 v205, 0x37800000, v204
	v_cndmask_b32_e32 v204, v204, v205, vcc
	v_cmp_class_f32_e32 vcc, v170, v196
	s_nop 1
	v_cndmask_b32_e32 v170, v204, v170, vcc
	v_div_scale_f32 v204, s[4:5], v170, v170, v200
	v_rcp_f32_e32 v205, v204
	s_mov_b64 s[4:5], -1
	v_fma_f32 v206, -v204, v205, 1.0
	v_fmac_f32_e32 v205, v206, v205
	v_div_scale_f32 v206, vcc, v200, v170, v200
	v_mul_f32_e32 v207, v206, v205
	v_fma_f32 v208, -v204, v207, v206
	v_fmac_f32_e32 v207, v208, v205
	v_fma_f32 v204, -v204, v207, v206
	v_div_fmas_f32 v204, v204, v205, v207
	v_div_fixup_f32 v170, v204, v170, v200
	v_pk_mul_f32 v[216:217], v[26:27], v[170:171] op_sel_hi:[1,0]
	v_pk_mul_f32 v[210:211], v[50:51], v[170:171] op_sel_hi:[1,0]
	v_pk_mul_f32 v[216:217], v[130:131], v[216:217]
	v_pk_mul_f32 v[210:211], v[138:139], v[210:211]
	v_pk_mul_f32 v[214:215], v[32:33], v[170:171] op_sel_hi:[1,0]
	s_waitcnt lgkmcnt(0)
	v_pk_mul_f32 v[224:225], v[146:147], v[216:217]
	v_pk_mul_f32 v[204:205], v[56:57], v[170:171] op_sel_hi:[1,0]
	s_waitcnt lgkmcnt(0)
	v_pk_fma_f32 v[224:225], v[154:155], v[210:211], v[224:225] neg_lo:[0,0,1] neg_hi:[0,0,1]
	v_pk_mul_f32 v[154:155], v[154:155], v[216:217]
	v_pk_mul_f32 v[212:213], v[30:31], v[170:171] op_sel_hi:[1,0]
	v_pk_mul_f32 v[214:215], v[136:137], v[214:215]
	v_pk_mul_f32 v[218:219], v[28:29], v[170:171] op_sel_hi:[1,0]
	v_pk_fma_f32 v[154:155], v[146:147], v[210:211], v[154:155]
	v_lshlrev_b32_e32 v146, 6, v228
	v_lshlrev_b32_e32 v147, 3, v228
	v_pk_mul_f32 v[206:207], v[54:55], v[170:171] op_sel_hi:[1,0]
	v_pk_mul_f32 v[204:205], v[144:145], v[204:205]
	v_pk_mul_f32 v[208:209], v[52:53], v[170:171] op_sel_hi:[1,0]
	v_pk_mul_f32 v[212:213], v[134:135], v[212:213]
	v_pk_mul_f32 v[218:219], v[132:133], v[218:219]
	v_pk_mul_f32 v[222:223], v[152:153], v[214:215]
	v_and_b32_e32 v146, 0x1f000, v146
	v_and_b32_e32 v147, 0xf8, v147
	v_pk_mul_f32 v[206:207], v[142:143], v[206:207]
	v_pk_mul_f32 v[208:209], v[140:141], v[208:209]
	v_pk_mul_f32 v[220:221], v[150:151], v[212:213]
	s_waitcnt lgkmcnt(0)
	v_pk_fma_f32 v[222:223], v[160:161], v[204:205], v[222:223] neg_lo:[0,0,1] neg_hi:[0,0,1]
	v_pk_mul_f32 v[226:227], v[148:149], v[218:219]
	v_pk_mul_f32 v[160:161], v[160:161], v[214:215]
	v_or3_b32 v146, v146, v147, v184
	v_pk_fma_f32 v[220:221], v[158:159], v[206:207], v[220:221] neg_lo:[0,0,1] neg_hi:[0,0,1]
	v_pk_fma_f32 v[226:227], v[156:157], v[208:209], v[226:227] neg_lo:[0,0,1] neg_hi:[0,0,1]
	v_pk_mul_f32 v[158:159], v[158:159], v[212:213]
	v_pk_fma_f32 v[152:153], v[152:153], v[204:205], v[160:161]
	v_pk_mul_f32 v[156:157], v[156:157], v[218:219]
	v_ashrrev_i32_e32 v147, 31, v146
	v_add_u32_e32 v204, 0xa0, v199
	v_pk_fma_f32 v[150:151], v[150:151], v[206:207], v[158:159]
	v_pk_fma_f32 v[156:157], v[148:149], v[208:209], v[156:157]
	v_lshl_add_u64 v[158:159], v[146:147], 1, s[54:55]
	v_cvt_pk_f16_f32 v146, v220, v221
	v_cvt_pk_f16_f32 v147, v222, v223
	v_cvt_pk_f16_f32 v148, v224, v225
	v_cvt_pk_f16_f32 v149, v226, v227
	v_and_b32_e32 v184, 0x7ef, v204
	v_cvt_pk_f16_f32 v150, v150, v151
	v_cvt_pk_f16_f32 v151, v152, v153
	v_cvt_pk_f16_f32 v152, v154, v155
	v_cvt_pk_f16_f32 v153, v156, v157
	global_store_dwordx4 v[158:159], v[146:149], off sc1
	v_lshlrev_b32_e32 v170, 7, v184
	v_mul_f32_e32 v205, v41, v41
	v_lshl_add_u64 v[146:147], v[158:159], 0, s[10:11]
	global_store_dwordx4 v[146:147], v[150:153], off sc1
	v_pk_mul_f32 v[206:207], v[36:37], v[36:37]
	ds_read_b128 v[146:149], v245 offset:3072
	ds_read_b128 v[154:157], v244 offset:3072
	s_nop 0
	ds_read_b128 v[150:153], v245 offset:35840
	s_nop 0
	ds_read_b128 v[158:161], v244 offset:35840
	v_mul_f32_e32 v170, v39, v39
	v_pk_mul_f32 v[208:209], v[34:35], v[34:35]
	v_fmac_f32_e32 v170, v38, v38
	v_fmac_f32_e32 v205, v40, v40
	v_mov_b32_e32 v210, v206
	v_mov_b32_e32 v211, v208
	v_mov_b32_e32 v208, v207
	v_add_f32_e32 v170, v170, v205
	v_pk_add_f32 v[206:207], v[210:211], v[208:209]
	v_pk_mul_f32 v[208:209], v[14:15], v[14:15]
	v_add_f32_e32 v170, v170, v207
	v_add_f32_e32 v170, v206, v170
	v_pk_mul_f32 v[206:207], v[16:17], v[16:17]
	v_mov_b32_e32 v211, v208
	v_mov_b32_e32 v210, v206
	v_mov_b32_e32 v208, v207
	v_pk_add_f32 v[206:207], v[210:211], v[208:209]
	v_pk_mul_f32 v[208:209], v[10:11], v[10:11]
	v_add_f32_e32 v170, v170, v207
	v_add_f32_e32 v170, v206, v170
	v_pk_mul_f32 v[206:207], v[12:13], v[12:13]
	v_mov_b32_e32 v211, v208
	v_mov_b32_e32 v210, v206
	v_mov_b32_e32 v208, v207
	v_pk_add_f32 v[206:207], v[210:211], v[208:209]
	s_andn2_b64 vcc, exec, s[52:53]
	v_add_f32_e32 v170, v207, v170
	v_add_f32_e32 v170, v206, v170
	v_mov_b32_e32 v205, v170
	s_nop 1
	v_permlane16_swap_b32_e32 v205, v170
	v_lshlrev_b32_e32 v206, 6, v184
	s_waitcnt lgkmcnt(0)
	v_add_f32_e32 v170, v170, v205
	v_mov_b32_e32 v205, v170
	s_nop 1
	v_permlane32_swap_b32_e32 v205, v170
	s_cbranch_vccnz .LBB1_22
	v_lshlrev_b32_e32 v204, 3, v204
	v_and_b32_e32 v184, 0x1f000, v206
	v_and_b32_e32 v204, 0x178, v204
	v_or3_b32 v184, v184, v204, v203
	s_mov_b64 s[4:5], 0

.LBB1_25:
	s_waitcnt lgkmcnt(0)
	v_add_f32_e32 v170, v170, v205
	v_fmamk_f32 v170, v170, 0x3c800000, v195
	v_mul_f32_e32 v185, 0x4f800000, v170
	v_cmp_gt_f32_e32 vcc, s70, v170
	s_lshl_b32 s10, s8, 1
	s_nop 0
	v_cndmask_b32_e32 v170, v170, v185, vcc
	v_sqrt_f32_e32 v185, v170
	s_nop 0
	v_add_u32_e32 v204, -1, v185
	v_fma_f32 v206, -v204, v185, v170
	v_add_u32_e32 v205, 1, v185
	v_cmp_ge_f32_e64 s[4:5], 0, v206
	s_nop 1
	v_cndmask_b32_e64 v204, v185, v204, s[4:5]
	v_fma_f32 v185, -v205, v185, v170
	v_cmp_lt_f32_e64 s[4:5], 0, v185
	s_nop 1
	v_cndmask_b32_e64 v185, v204, v205, s[4:5]
	v_mul_f32_e32 v204, 0x37800000, v185
	v_cndmask_b32_e32 v185, v185, v204, vcc
	v_cmp_class_f32_e32 vcc, v170, v196
	s_nop 1
	v_cndmask_b32_e32 v170, v185, v170, vcc
	v_div_scale_f32 v185, s[4:5], v170, v170, v200
	v_rcp_f32_e32 v204, v185
	s_nop 0
	v_fma_f32 v205, -v185, v204, 1.0
	v_fmac_f32_e32 v204, v205, v204
	v_div_scale_f32 v205, vcc, v200, v170, v200
	v_mul_f32_e32 v206, v205, v204
	v_fma_f32 v207, -v185, v206, v205
	v_fmac_f32_e32 v206, v207, v204
	v_fma_f32 v185, -v185, v206, v205
	v_div_fmas_f32 v185, v185, v204, v206
	v_div_fixup_f32 v170, v185, v170, v200
	v_pk_mul_f32 v[212:213], v[14:15], v[170:171] op_sel_hi:[1,0]
	v_pk_mul_f32 v[214:215], v[16:17], v[170:171] op_sel_hi:[1,0]
	v_pk_mul_f32 v[216:217], v[10:11], v[170:171] op_sel_hi:[1,0]
	v_pk_mul_f32 v[218:219], v[12:13], v[170:171] op_sel_hi:[1,0]
	v_pk_mul_f32 v[204:205], v[40:41], v[170:171] op_sel_hi:[1,0]
	v_pk_mul_f32 v[206:207], v[38:39], v[170:171] op_sel_hi:[1,0]
	v_pk_mul_f32 v[208:209], v[36:37], v[170:171] op_sel_hi:[1,0]
	v_pk_mul_f32 v[210:211], v[34:35], v[170:171] op_sel_hi:[1,0]
	v_pk_mul_f32 v[214:215], v[136:137], v[214:215]
	v_pk_mul_f32 v[212:213], v[134:135], v[212:213]
	v_pk_mul_f32 v[218:219], v[132:133], v[218:219]
	v_pk_mul_f32 v[216:217], v[130:131], v[216:217]
	v_pk_mul_f32 v[206:207], v[142:143], v[206:207]
	v_pk_mul_f32 v[204:205], v[144:145], v[204:205]
	v_pk_mul_f32 v[210:211], v[138:139], v[210:211]
	v_pk_mul_f32 v[208:209], v[140:141], v[208:209]
	s_waitcnt lgkmcnt(0)
	v_pk_mul_f32 v[220:221], v[158:159], v[212:213]
	v_pk_mul_f32 v[222:223], v[160:161], v[214:215]
	v_pk_mul_f32 v[224:225], v[150:151], v[216:217]
	v_pk_mul_f32 v[226:227], v[152:153], v[218:219]
	v_pk_fma_f32 v[222:223], v[156:157], v[204:205], v[222:223] neg_lo:[0,0,1] neg_hi:[0,0,1]
	v_pk_fma_f32 v[220:221], v[154:155], v[206:207], v[220:221] neg_lo:[0,0,1] neg_hi:[0,0,1]
	v_pk_fma_f32 v[226:227], v[148:149], v[208:209], v[226:227] neg_lo:[0,0,1] neg_hi:[0,0,1]
	v_pk_fma_f32 v[224:225], v[146:147], v[210:211], v[224:225] neg_lo:[0,0,1] neg_hi:[0,0,1]
	v_pk_mul_f32 v[154:155], v[154:155], v[212:213]
	v_pk_mul_f32 v[156:157], v[156:157], v[214:215]
	v_pk_mul_f32 v[146:147], v[146:147], v[216:217]
	v_pk_mul_f32 v[148:149], v[148:149], v[218:219]
	v_ashrrev_i32_e32 v185, 31, v184
	v_pk_fma_f32 v[156:157], v[160:161], v[204:205], v[156:157]
	v_pk_fma_f32 v[154:155], v[158:159], v[206:207], v[154:155]
	v_pk_fma_f32 v[158:159], v[152:153], v[208:209], v[148:149]
	v_pk_fma_f32 v[152:153], v[150:151], v[210:211], v[146:147]
	v_lshl_add_u64 v[160:161], v[184:185], 1, s[6:7]
	v_cvt_pk_f16_f32 v146, v220, v221
	v_cvt_pk_f16_f32 v147, v222, v223
	v_cvt_pk_f16_f32 v148, v224, v225
	v_cvt_pk_f16_f32 v149, v226, v227
	v_cvt_pk_f16_f32 v150, v154, v155
	v_cvt_pk_f16_f32 v151, v156, v157
	v_cvt_pk_f16_f32 v152, v152, v153
	v_cvt_pk_f16_f32 v153, v158, v159
	global_store_dwordx4 v[160:161], v[146:149], off sc1
	v_add_u32_e32 v208, 0xb0, v199
	v_and_b32_e32 v209, 0x7ff, v208
	v_lshl_add_u64 v[146:147], v[160:161], 0, s[10:11]
	global_store_dwordx4 v[146:147], v[150:153], off sc1
	v_mul_f32_e32 v146, v23, v23
	v_mul_f32_e32 v147, v25, v25
	v_fmac_f32_e32 v146, v22, v22
	v_fmac_f32_e32 v147, v24, v24
	v_add_f32_e32 v152, v146, v147
	v_pk_mul_f32 v[146:147], v[20:21], v[20:21]
	v_pk_mul_f32 v[148:149], v[18:19], v[18:19]
	v_mov_b32_e32 v150, v146
	v_mov_b32_e32 v151, v148
	v_mov_b32_e32 v148, v147
	v_pk_add_f32 v[146:147], v[150:151], v[148:149]
	v_lshlrev_b32_e32 v170, 7, v209
	v_add_f32_e32 v147, v152, v147
	v_add_f32_e32 v210, v146, v147
	ds_read_b128 v[146:149], v245 offset:52224
	s_nop 0
	ds_read_b128 v[150:153], v244 offset:52224
	s_nop 0
	ds_read_b128 v[154:157], v245 offset:19456
	s_nop 0
	ds_read_b128 v[158:161], v244 offset:19456
	v_pk_mul_f32 v[184:185], v[8:9], v[8:9]
	v_pk_mul_f32 v[204:205], v[6:7], v[6:7]
	v_mov_b32_e32 v206, v184
	v_mov_b32_e32 v207, v204
	v_mov_b32_e32 v204, v185
	v_pk_add_f32 v[184:185], v[206:207], v[204:205]
	v_pk_mul_f32 v[204:205], v[2:3], v[2:3]
	v_add_f32_e32 v170, v210, v185
	v_add_f32_e32 v170, v184, v170
	v_pk_mul_f32 v[184:185], v[4:5], v[4:5]
	v_mov_b32_e32 v207, v204
	v_mov_b32_e32 v206, v184
	v_mov_b32_e32 v204, v185
	v_pk_add_f32 v[184:185], v[206:207], v[204:205]
	s_nop 0
	v_add_f32_e32 v170, v185, v170
	v_add_f32_e32 v170, v184, v170
	v_mov_b32_e32 v184, v170
	s_nop 1
	v_permlane16_swap_b32_e32 v184, v170
	s_waitcnt lgkmcnt(0)
	v_add_f32_e32 v170, v170, v184
	v_mov_b32_e32 v184, v170
	s_nop 1
	v_permlane32_swap_b32_e32 v184, v170
	s_waitcnt lgkmcnt(0)
	v_add_f32_e32 v170, v170, v184
	v_fmamk_f32 v170, v170, 0x3c800000, v195
	v_mul_f32_e32 v184, 0x4f800000, v170
	v_cmp_gt_f32_e32 vcc, s70, v170
	s_nop 1
	v_cndmask_b32_e32 v170, v170, v184, vcc
	v_sqrt_f32_e32 v184, v170
	s_nop 0
	v_add_u32_e32 v185, -1, v184
	v_fma_f32 v201, -v185, v184, v170
	v_cmp_ge_f32_e64 s[4:5], 0, v201
	v_add_u32_e32 v201, 1, v184
	s_nop 0
	v_cndmask_b32_e64 v185, v184, v185, s[4:5]
	v_fma_f32 v184, -v201, v184, v170
	v_cmp_lt_f32_e64 s[4:5], 0, v184
	s_nop 1
	v_cndmask_b32_e64 v184, v185, v201, s[4:5]
	v_mul_f32_e32 v185, 0x37800000, v184
	v_cndmask_b32_e32 v184, v184, v185, vcc
	v_cmp_class_f32_e32 vcc, v170, v196
	s_nop 1
	v_cndmask_b32_e32 v170, v184, v170, vcc
	v_div_scale_f32 v184, s[4:5], v170, v170, v200
	v_rcp_f32_e32 v185, v184
	s_nop 0
	v_fma_f32 v201, -v184, v185, 1.0
	v_fmac_f32_e32 v185, v201, v185
	v_div_scale_f32 v201, vcc, v200, v170, v200
	v_mul_f32_e32 v202, v201, v185
	v_fma_f32 v204, -v184, v202, v201
	v_fmac_f32_e32 v202, v204, v185
	v_fma_f32 v184, -v184, v202, v201
	v_div_fmas_f32 v184, v184, v185, v202
	v_div_fixup_f32 v170, v184, v170, v200
	v_pk_mul_f32 v[184:185], v[24:25], v[170:171] op_sel_hi:[1,0]
	v_pk_mul_f32 v[200:201], v[22:23], v[170:171] op_sel_hi:[1,0]
	v_pk_mul_f32 v[144:145], v[144:145], v[184:185]
	v_pk_mul_f32 v[184:185], v[20:21], v[170:171] op_sel_hi:[1,0]
	v_pk_mul_f32 v[142:143], v[142:143], v[200:201]
	v_pk_mul_f32 v[140:141], v[140:141], v[184:185]
	v_pk_mul_f32 v[184:185], v[6:7], v[170:171] op_sel_hi:[1,0]
	v_pk_mul_f32 v[200:201], v[18:19], v[170:171] op_sel_hi:[1,0]
	v_pk_mul_f32 v[134:135], v[134:135], v[184:185]
	v_pk_mul_f32 v[184:185], v[2:3], v[170:171] op_sel_hi:[1,0]
	v_pk_mul_f32 v[138:139], v[138:139], v[200:201]
	v_pk_mul_f32 v[130:131], v[130:131], v[184:185]
	v_pk_mul_f32 v[200:201], v[8:9], v[170:171] op_sel_hi:[1,0]
	s_waitcnt lgkmcnt(0)
	v_pk_mul_f32 v[204:205], v[146:147], v[130:131]
	s_waitcnt lgkmcnt(0)
	v_pk_mul_f32 v[130:131], v[154:155], v[130:131]
	v_pk_mul_f32 v[136:137], v[136:137], v[200:201]
	v_pk_mul_f32 v[200:201], v[4:5], v[170:171] op_sel_hi:[1,0]
	v_pk_fma_f32 v[204:205], v[154:155], v[138:139], v[204:205] neg_lo:[0,0,1] neg_hi:[0,0,1]
	v_pk_fma_f32 v[138:139], v[146:147], v[138:139], v[130:131]
	v_lshlrev_b32_e32 v130, 6, v209
	v_lshlrev_b32_e32 v131, 3, v208
	v_pk_mul_f32 v[132:133], v[132:133], v[200:201]
	v_and_b32_e32 v130, s37, v130
	v_and_b32_e32 v131, s9, v131
	v_pk_mul_f32 v[184:185], v[150:151], v[134:135]
	v_pk_mul_f32 v[200:201], v[152:153], v[136:137]
	v_pk_mul_f32 v[206:207], v[148:149], v[132:133]
	v_or3_b32 v130, v131, v203, v130
	s_waitcnt lgkmcnt(0)
	v_pk_fma_f32 v[200:201], v[160:161], v[144:145], v[200:201] neg_lo:[0,0,1] neg_hi:[0,0,1]
	v_pk_fma_f32 v[184:185], v[158:159], v[142:143], v[184:185] neg_lo:[0,0,1] neg_hi:[0,0,1]
	v_pk_fma_f32 v[206:207], v[156:157], v[140:141], v[206:207] neg_lo:[0,0,1] neg_hi:[0,0,1]
	v_pk_mul_f32 v[134:135], v[158:159], v[134:135]
	v_pk_mul_f32 v[136:137], v[160:161], v[136:137]
	v_pk_mul_f32 v[132:133], v[156:157], v[132:133]
	v_ashrrev_i32_e32 v131, 31, v130
	v_pk_fma_f32 v[136:137], v[152:153], v[144:145], v[136:137]
	v_pk_fma_f32 v[134:135], v[150:151], v[142:143], v[134:135]
	v_pk_fma_f32 v[140:141], v[148:149], v[140:141], v[132:133]
	v_lshl_add_u64 v[142:143], v[130:131], 1, s[6:7]
	v_cvt_pk_f16_f32 v130, v184, v185
	v_cvt_pk_f16_f32 v131, v200, v201
	v_cvt_pk_f16_f32 v132, v204, v205
	v_cvt_pk_f16_f32 v133, v206, v207
	v_cvt_pk_f16_f32 v134, v134, v135
	v_cvt_pk_f16_f32 v135, v136, v137
	v_cvt_pk_f16_f32 v136, v138, v139
	v_cvt_pk_f16_f32 v137, v140, v141
	global_store_dwordx4 v[142:143], v[130:133], off sc1
	s_nop 1
	v_lshl_add_u64 v[130:131], v[142:143], 0, s[10:11]
	global_store_dwordx4 v[130:131], v[134:137], off sc1
	s_branch .LBB1_14
